# layer-1 out-GEMM epilogue (EpiOut bf16 residual): the 15 later residual row-group loads hoisted to the epilogue top into dead K-loop operand registers, per-group wait vmcnt(1)->vmcnt(15)
# baseline (speedup 1.0000x reference)
.LBB0_2805:
	v_lshl_add_u32 v124, v120, 8, v172
	v_ashrrev_i32_e32 v125, 31, v124
	v_lshl_or_b32 v122, v122, 8, v171
	v_lshlrev_b64 v[124:125], 11, v[124:125]
	v_lshrrev_b32_e32 v121, 4, v120
	s_movk_i32 s52, 0x80
	v_ashrrev_i32_e32 v123, 31, v122
	v_lshl_add_u64 v[124:125], s[24:25], 0, v[124:125]
	v_mul_lo_u32 v121, v121, s91
	v_cmp_gt_i32_e32 vcc, s52, v120
	v_lshl_add_u64 v[168:169], v[122:123], 1, v[124:125]
	global_load_dwordx4 v[176:179], v[168:169], off
	v_cndmask_b32_e32 v120, v175, v121, vcc
	v_ashrrev_i32_e32 v121, 31, v120
	v_lshl_add_u64 v[120:121], v[120:121], 2, s[26:27]
	v_lshl_add_u64 v[124:125], v[122:123], 2, v[120:121]
	global_load_dwordx4 v[132:135], v[124:125], off
	global_load_dwordx4 v[128:131], v[124:125], off offset:16
	global_load_dwordx4 v[120:123], v[124:125], off offset:528
	s_nop 0
	global_load_dwordx4 v[124:127], v[124:125], off offset:512
	global_load_dwordx4 v[184:187], v[168:169], off offset:256
	s_mov_b32 s52, 0x8000
	v_add_co_u32_e32 v246, vcc, s52, v168
	v_addc_co_u32_e32 v247, vcc, 0, v169, vcc
	global_load_dwordx4 v[188:191], v[246:247], off
	global_load_dwordx4 v[192:195], v[246:247], off offset:256
	s_mov_b32 s52, 0x10000
	v_add_co_u32_e32 v244, vcc, s52, v168
	v_addc_co_u32_e32 v245, vcc, 0, v169, vcc
	global_load_dwordx4 v[196:199], v[244:245], off
	global_load_dwordx4 v[200:203], v[244:245], off offset:256
	s_mov_b32 s52, 0x18000
	v_add_co_u32_e32 v246, vcc, s52, v168
	v_addc_co_u32_e32 v247, vcc, 0, v169, vcc
	global_load_dwordx4 v[204:207], v[246:247], off
	global_load_dwordx4 v[208:211], v[246:247], off offset:256
	s_mov_b32 s52, 0x40000
	v_add_co_u32_e32 v244, vcc, s52, v168
	v_addc_co_u32_e32 v245, vcc, 0, v169, vcc
	global_load_dwordx4 v[212:215], v[244:245], off
	global_load_dwordx4 v[216:219], v[244:245], off offset:256
	s_mov_b32 s52, 0x48000
	v_add_co_u32_e32 v246, vcc, s52, v168
	v_addc_co_u32_e32 v247, vcc, 0, v169, vcc
	global_load_dwordx4 v[220:223], v[246:247], off
	global_load_dwordx4 v[224:227], v[246:247], off offset:256
	s_mov_b32 s52, 0x50000
	v_add_co_u32_e32 v244, vcc, s52, v168
	v_addc_co_u32_e32 v245, vcc, 0, v169, vcc
	global_load_dwordx4 v[228:231], v[244:245], off
	global_load_dwordx4 v[232:235], v[244:245], off offset:256
	s_mov_b32 s52, 0x58000
	v_add_co_u32_e32 v246, vcc, s52, v168
	v_addc_co_u32_e32 v247, vcc, 0, v169, vcc
	global_load_dwordx4 v[236:239], v[246:247], off
	global_load_dwordx4 v[240:243], v[246:247], off offset:256
	s_mov_b32 s52, 0x8000
	s_mov_b64 s[54:55], -1
	s_waitcnt vmcnt(15)
	v_lshlrev_b32_e32 v180, 16, v176
	v_and_b32_e32 v181, 0xffff0000, v176
	v_lshlrev_b32_e32 v176, 16, v177
	v_and_b32_e32 v177, 0xffff0000, v177
	v_lshlrev_b32_e32 v182, 16, v178
	v_and_b32_e32 v183, 0xffff0000, v178
	v_lshlrev_b32_e32 v178, 16, v179
	v_and_b32_e32 v179, 0xffff0000, v179
	v_pk_fma_f32 v[142:143], v[142:143], v[134:135], v[176:177]
	v_pk_fma_f32 v[140:141], v[140:141], v[132:133], v[180:181]
	v_pk_fma_f32 v[176:177], v[138:139], v[130:131], v[178:179]
	v_pk_fma_f32 v[138:139], v[136:137], v[128:129], v[182:183]
	v_cvt_pk_bf16_f32 v136, v140, v141
	v_cvt_pk_bf16_f32 v137, v142, v143
	s_nop 0
	v_cvt_pk_bf16_f32 v138, v138, v139
	v_cvt_pk_bf16_f32 v139, v176, v177
	v_add_co_u32_e32 v176, vcc, s52, v168
	global_store_dwordx4 v[168:169], v[136:139], off
	s_nop 0
	v_addc_co_u32_e32 v177, vcc, 0, v169, vcc
	s_mov_b32 s52, 0x10000
	s_waitcnt vmcnt(15)
	v_lshlrev_b32_e32 v136, 16, v184
	v_and_b32_e32 v137, 0xffff0000, v184
	v_lshlrev_b32_e32 v138, 16, v185
	v_and_b32_e32 v139, 0xffff0000, v185
	v_lshlrev_b32_e32 v140, 16, v186
	v_and_b32_e32 v141, 0xffff0000, v186
	v_lshlrev_b32_e32 v142, 16, v187
	v_and_b32_e32 v143, 0xffff0000, v187
	v_pk_fma_f32 v[118:119], v[118:119], v[126:127], v[138:139]
	v_pk_fma_f32 v[116:117], v[116:117], v[124:125], v[136:137]
	v_pk_fma_f32 v[136:137], v[110:111], v[122:123], v[142:143]
	v_pk_fma_f32 v[110:111], v[108:109], v[120:121], v[140:141]
	v_cvt_pk_bf16_f32 v108, v116, v117
	v_cvt_pk_bf16_f32 v109, v118, v119
	s_nop 0
	v_cvt_pk_bf16_f32 v110, v110, v111
	v_cvt_pk_bf16_f32 v111, v136, v137
	v_lshl_add_u64 v[136:137], v[168:169], 0, s[40:41]
	global_store_dwordx4 v[168:169], v[108:111], off offset:256
	s_waitcnt vmcnt(15)
	s_nop 0
	v_lshlrev_b32_e32 v108, 16, v188
	v_and_b32_e32 v109, 0xffff0000, v188
	v_lshlrev_b32_e32 v110, 16, v189
	v_and_b32_e32 v111, 0xffff0000, v189
	v_lshlrev_b32_e32 v116, 16, v190
	v_and_b32_e32 v117, 0xffff0000, v190
	v_lshlrev_b32_e32 v118, 16, v191
	v_and_b32_e32 v119, 0xffff0000, v191
	v_pk_fma_f32 v[110:111], v[114:115], v[134:135], v[110:111]
	v_pk_fma_f32 v[108:109], v[112:113], v[132:133], v[108:109]
	v_pk_fma_f32 v[112:113], v[106:107], v[130:131], v[118:119]
	v_pk_fma_f32 v[106:107], v[104:105], v[128:129], v[116:117]
	v_cvt_pk_bf16_f32 v104, v108, v109
	v_cvt_pk_bf16_f32 v105, v110, v111
	s_nop 0
	v_cvt_pk_bf16_f32 v106, v106, v107
	v_cvt_pk_bf16_f32 v107, v112, v113
	v_add_co_u32_e32 v112, vcc, s52, v168
	global_store_dwordx4 v[176:177], v[104:107], off
	s_nop 0
	v_addc_co_u32_e32 v113, vcc, 0, v169, vcc
	s_mov_b32 s52, 0x18000
	s_waitcnt vmcnt(15)
	v_lshlrev_b32_e32 v104, 16, v192
	v_and_b32_e32 v105, 0xffff0000, v192
	v_lshlrev_b32_e32 v106, 16, v193
	v_and_b32_e32 v107, 0xffff0000, v193
	v_lshlrev_b32_e32 v108, 16, v194
	v_and_b32_e32 v109, 0xffff0000, v194
	v_lshlrev_b32_e32 v110, 16, v195
	v_and_b32_e32 v111, 0xffff0000, v195
	v_pk_fma_f32 v[102:103], v[102:103], v[126:127], v[106:107]
	v_pk_fma_f32 v[100:101], v[100:101], v[124:125], v[104:105]
	v_pk_fma_f32 v[104:105], v[94:95], v[122:123], v[110:111]
	v_pk_fma_f32 v[94:95], v[92:93], v[120:121], v[108:109]
	v_cvt_pk_bf16_f32 v92, v100, v101
	v_cvt_pk_bf16_f32 v93, v102, v103
	s_nop 0
	v_cvt_pk_bf16_f32 v94, v94, v95
	v_cvt_pk_bf16_f32 v95, v104, v105
	v_lshl_add_u64 v[104:105], v[168:169], 0, s[42:43]
	global_store_dwordx4 v[136:137], v[92:95], off offset:256
	s_waitcnt vmcnt(15)
	s_nop 0
	v_lshlrev_b32_e32 v92, 16, v196
	v_and_b32_e32 v93, 0xffff0000, v196
	v_lshlrev_b32_e32 v94, 16, v197
	v_and_b32_e32 v95, 0xffff0000, v197
	v_lshlrev_b32_e32 v100, 16, v198
	v_and_b32_e32 v101, 0xffff0000, v198
	v_lshlrev_b32_e32 v102, 16, v199
	v_and_b32_e32 v103, 0xffff0000, v199
	v_pk_fma_f32 v[94:95], v[98:99], v[134:135], v[94:95]
	v_pk_fma_f32 v[92:93], v[96:97], v[132:133], v[92:93]
	v_pk_fma_f32 v[96:97], v[90:91], v[130:131], v[102:103]
	v_pk_fma_f32 v[90:91], v[88:89], v[128:129], v[100:101]
	v_cvt_pk_bf16_f32 v88, v92, v93
	v_cvt_pk_bf16_f32 v89, v94, v95
	s_nop 0
	v_cvt_pk_bf16_f32 v90, v90, v91
	v_cvt_pk_bf16_f32 v91, v96, v97
	v_add_co_u32_e32 v96, vcc, s52, v168
	global_store_dwordx4 v[112:113], v[88:91], off
	s_nop 0
	v_addc_co_u32_e32 v97, vcc, 0, v169, vcc
	s_waitcnt vmcnt(15)
	v_lshlrev_b32_e32 v88, 16, v200
	v_and_b32_e32 v89, 0xffff0000, v200
	v_lshlrev_b32_e32 v90, 16, v201
	v_and_b32_e32 v91, 0xffff0000, v201
	v_lshlrev_b32_e32 v92, 16, v202
	v_and_b32_e32 v93, 0xffff0000, v202
	v_lshlrev_b32_e32 v94, 16, v203
	v_and_b32_e32 v95, 0xffff0000, v203
	v_pk_fma_f32 v[86:87], v[86:87], v[126:127], v[90:91]
	v_pk_fma_f32 v[84:85], v[84:85], v[124:125], v[88:89]
	v_pk_fma_f32 v[88:89], v[78:79], v[122:123], v[94:95]
	v_pk_fma_f32 v[78:79], v[76:77], v[120:121], v[92:93]
	v_cvt_pk_bf16_f32 v76, v84, v85
	v_cvt_pk_bf16_f32 v77, v86, v87
	s_nop 0
	v_cvt_pk_bf16_f32 v78, v78, v79
	v_cvt_pk_bf16_f32 v79, v88, v89
	v_lshl_add_u64 v[88:89], v[168:169], 0, s[44:45]
	global_store_dwordx4 v[104:105], v[76:79], off offset:256
	s_waitcnt vmcnt(15)
	s_nop 0
	v_lshlrev_b32_e32 v76, 16, v204
	v_and_b32_e32 v77, 0xffff0000, v204
	v_lshlrev_b32_e32 v78, 16, v205
	v_and_b32_e32 v79, 0xffff0000, v205
	v_lshlrev_b32_e32 v84, 16, v206
	v_and_b32_e32 v85, 0xffff0000, v206
	v_lshlrev_b32_e32 v86, 16, v207
	v_and_b32_e32 v87, 0xffff0000, v207
	v_pk_fma_f32 v[78:79], v[82:83], v[134:135], v[78:79]
	v_pk_fma_f32 v[76:77], v[80:81], v[132:133], v[76:77]
	v_pk_fma_f32 v[80:81], v[74:75], v[130:131], v[86:87]
	v_pk_fma_f32 v[74:75], v[72:73], v[128:129], v[84:85]
	v_cvt_pk_bf16_f32 v72, v76, v77
	v_cvt_pk_bf16_f32 v73, v78, v79
	s_nop 0
	v_cvt_pk_bf16_f32 v74, v74, v75
	v_cvt_pk_bf16_f32 v75, v80, v81
	v_add_co_u32_e32 v80, vcc, s92, v168
	global_store_dwordx4 v[96:97], v[72:75], off
	s_nop 0
	v_addc_co_u32_e32 v81, vcc, 0, v169, vcc
	s_waitcnt vmcnt(15)
	v_lshlrev_b32_e32 v72, 16, v208
	v_and_b32_e32 v73, 0xffff0000, v208
	v_lshlrev_b32_e32 v74, 16, v209
	v_and_b32_e32 v75, 0xffff0000, v209
	v_lshlrev_b32_e32 v76, 16, v210
	v_and_b32_e32 v77, 0xffff0000, v210
	v_lshlrev_b32_e32 v78, 16, v211
	v_and_b32_e32 v79, 0xffff0000, v211
	v_pk_fma_f32 v[70:71], v[70:71], v[126:127], v[74:75]
	v_pk_fma_f32 v[68:69], v[68:69], v[124:125], v[72:73]
	v_pk_fma_f32 v[72:73], v[66:67], v[122:123], v[78:79]
	v_pk_fma_f32 v[66:67], v[64:65], v[120:121], v[76:77]
	v_cvt_pk_bf16_f32 v64, v68, v69
	v_cvt_pk_bf16_f32 v65, v70, v71
	s_nop 0
	v_cvt_pk_bf16_f32 v66, v66, v67
	v_cvt_pk_bf16_f32 v67, v72, v73
	v_lshl_add_u64 v[72:73], v[168:169], 0, s[10:11]
	global_store_dwordx4 v[88:89], v[64:67], off offset:256
	s_waitcnt vmcnt(15)
	s_nop 0
	v_lshlrev_b32_e32 v64, 16, v212
	v_and_b32_e32 v65, 0xffff0000, v212
	v_lshlrev_b32_e32 v66, 16, v213
	v_and_b32_e32 v67, 0xffff0000, v213
	v_lshlrev_b32_e32 v68, 16, v214
	v_and_b32_e32 v69, 0xffff0000, v214
	v_lshlrev_b32_e32 v70, 16, v215
	v_and_b32_e32 v71, 0xffff0000, v215
	v_pk_fma_f32 v[62:63], v[62:63], v[134:135], v[66:67]
	v_pk_fma_f32 v[60:61], v[60:61], v[132:133], v[64:65]
	v_pk_fma_f32 v[64:65], v[58:59], v[130:131], v[70:71]
	v_pk_fma_f32 v[58:59], v[56:57], v[128:129], v[68:69]
	v_cvt_pk_bf16_f32 v56, v60, v61
	v_cvt_pk_bf16_f32 v57, v62, v63
	s_nop 0
	v_cvt_pk_bf16_f32 v58, v58, v59
	v_cvt_pk_bf16_f32 v59, v64, v65
	v_add_co_u32_e32 v64, vcc, s93, v168
	global_store_dwordx4 v[80:81], v[56:59], off
	s_nop 0
	v_addc_co_u32_e32 v65, vcc, 0, v169, vcc
	s_waitcnt vmcnt(15)
	v_lshlrev_b32_e32 v56, 16, v216
	v_and_b32_e32 v57, 0xffff0000, v216
	v_lshlrev_b32_e32 v58, 16, v217
	v_and_b32_e32 v59, 0xffff0000, v217
	v_lshlrev_b32_e32 v60, 16, v218
	v_and_b32_e32 v61, 0xffff0000, v218
	v_lshlrev_b32_e32 v62, 16, v219
	v_and_b32_e32 v63, 0xffff0000, v219
	v_pk_fma_f32 v[54:55], v[54:55], v[126:127], v[58:59]
	v_pk_fma_f32 v[52:53], v[52:53], v[124:125], v[56:57]
	v_pk_fma_f32 v[56:57], v[46:47], v[122:123], v[62:63]
	v_pk_fma_f32 v[46:47], v[44:45], v[120:121], v[60:61]
	v_cvt_pk_bf16_f32 v44, v52, v53
	v_cvt_pk_bf16_f32 v45, v54, v55
	s_nop 0
	v_cvt_pk_bf16_f32 v46, v46, v47
	v_cvt_pk_bf16_f32 v47, v56, v57
	v_lshl_add_u64 v[56:57], v[168:169], 0, s[46:47]
	global_store_dwordx4 v[72:73], v[44:47], off offset:256
	s_waitcnt vmcnt(15)
	s_nop 0
	v_lshlrev_b32_e32 v44, 16, v220
	v_and_b32_e32 v45, 0xffff0000, v220
	v_lshlrev_b32_e32 v46, 16, v221
	v_and_b32_e32 v47, 0xffff0000, v221
	v_lshlrev_b32_e32 v52, 16, v222
	v_and_b32_e32 v53, 0xffff0000, v222
	v_lshlrev_b32_e32 v54, 16, v223
	v_and_b32_e32 v55, 0xffff0000, v223
	v_pk_fma_f32 v[46:47], v[50:51], v[134:135], v[46:47]
	v_pk_fma_f32 v[44:45], v[48:49], v[132:133], v[44:45]
	v_pk_fma_f32 v[48:49], v[42:43], v[130:131], v[54:55]
	v_pk_fma_f32 v[42:43], v[40:41], v[128:129], v[52:53]
	v_cvt_pk_bf16_f32 v40, v44, v45
	v_cvt_pk_bf16_f32 v41, v46, v47
	s_nop 0
	v_cvt_pk_bf16_f32 v42, v42, v43
	v_cvt_pk_bf16_f32 v43, v48, v49
	v_add_co_u32_e32 v48, vcc, s94, v168
	global_store_dwordx4 v[64:65], v[40:43], off
	s_nop 0
	v_addc_co_u32_e32 v49, vcc, 0, v169, vcc
	s_waitcnt vmcnt(15)
	v_lshlrev_b32_e32 v40, 16, v224
	v_and_b32_e32 v41, 0xffff0000, v224
	v_lshlrev_b32_e32 v42, 16, v225
	v_and_b32_e32 v43, 0xffff0000, v225
	v_lshlrev_b32_e32 v44, 16, v226
	v_and_b32_e32 v45, 0xffff0000, v226
	v_lshlrev_b32_e32 v46, 16, v227
	v_and_b32_e32 v47, 0xffff0000, v227
	v_pk_fma_f32 v[38:39], v[38:39], v[126:127], v[42:43]
	v_pk_fma_f32 v[36:37], v[36:37], v[124:125], v[40:41]
	v_pk_fma_f32 v[40:41], v[30:31], v[122:123], v[46:47]
	v_pk_fma_f32 v[30:31], v[28:29], v[120:121], v[44:45]
	v_cvt_pk_bf16_f32 v28, v36, v37
	v_cvt_pk_bf16_f32 v29, v38, v39
	s_nop 0
	v_cvt_pk_bf16_f32 v30, v30, v31
	v_cvt_pk_bf16_f32 v31, v40, v41
	v_lshl_add_u64 v[40:41], v[168:169], 0, s[48:49]
	global_store_dwordx4 v[56:57], v[28:31], off offset:256
	s_waitcnt vmcnt(15)
	s_nop 0
	v_lshlrev_b32_e32 v28, 16, v228
	v_and_b32_e32 v29, 0xffff0000, v228
	v_lshlrev_b32_e32 v30, 16, v229
	v_and_b32_e32 v31, 0xffff0000, v229
	v_lshlrev_b32_e32 v36, 16, v230
	v_and_b32_e32 v37, 0xffff0000, v230
	v_lshlrev_b32_e32 v38, 16, v231
	v_and_b32_e32 v39, 0xffff0000, v231
	v_pk_fma_f32 v[30:31], v[34:35], v[134:135], v[30:31]
	v_pk_fma_f32 v[28:29], v[32:33], v[132:133], v[28:29]
	v_pk_fma_f32 v[32:33], v[26:27], v[130:131], v[38:39]
	v_pk_fma_f32 v[26:27], v[24:25], v[128:129], v[36:37]
	v_cvt_pk_bf16_f32 v24, v28, v29
	v_cvt_pk_bf16_f32 v25, v30, v31
	s_nop 0
	v_cvt_pk_bf16_f32 v26, v26, v27
	v_cvt_pk_bf16_f32 v27, v32, v33
	v_add_co_u32_e32 v32, vcc, s95, v168
	global_store_dwordx4 v[48:49], v[24:27], off
	s_nop 0
	v_addc_co_u32_e32 v33, vcc, 0, v169, vcc
	s_waitcnt vmcnt(15)
	v_lshlrev_b32_e32 v24, 16, v232
	v_and_b32_e32 v25, 0xffff0000, v232
	v_lshlrev_b32_e32 v26, 16, v233
	v_and_b32_e32 v27, 0xffff0000, v233
	v_lshlrev_b32_e32 v28, 16, v234
	v_and_b32_e32 v29, 0xffff0000, v234
	v_lshlrev_b32_e32 v30, 16, v235
	v_and_b32_e32 v31, 0xffff0000, v235
	v_pk_fma_f32 v[22:23], v[22:23], v[126:127], v[26:27]
	v_pk_fma_f32 v[20:21], v[20:21], v[124:125], v[24:25]
	v_pk_fma_f32 v[24:25], v[14:15], v[122:123], v[30:31]
	v_pk_fma_f32 v[14:15], v[12:13], v[120:121], v[28:29]
	v_cvt_pk_bf16_f32 v12, v20, v21
	v_cvt_pk_bf16_f32 v13, v22, v23
	s_nop 0
	v_cvt_pk_bf16_f32 v14, v14, v15
	v_cvt_pk_bf16_f32 v15, v24, v25
	v_lshl_add_u64 v[24:25], v[168:169], 0, s[50:51]
	global_store_dwordx4 v[40:41], v[12:15], off offset:256
	s_waitcnt vmcnt(15)
	s_nop 0
	v_lshlrev_b32_e32 v12, 16, v236
	v_and_b32_e32 v13, 0xffff0000, v236
	v_lshlrev_b32_e32 v14, 16, v237
	v_and_b32_e32 v15, 0xffff0000, v237
	v_lshlrev_b32_e32 v20, 16, v238
	v_and_b32_e32 v21, 0xffff0000, v238
	v_lshlrev_b32_e32 v22, 16, v239
	v_and_b32_e32 v23, 0xffff0000, v239
	v_pk_fma_f32 v[14:15], v[18:19], v[134:135], v[14:15]
	v_pk_fma_f32 v[12:13], v[16:17], v[132:133], v[12:13]
	v_pk_fma_f32 v[16:17], v[10:11], v[130:131], v[22:23]
	v_pk_fma_f32 v[10:11], v[8:9], v[128:129], v[20:21]
	v_cvt_pk_bf16_f32 v8, v12, v13
	v_cvt_pk_bf16_f32 v9, v14, v15
	s_nop 0
	v_cvt_pk_bf16_f32 v10, v10, v11
	v_cvt_pk_bf16_f32 v11, v16, v17
	s_nop 0
	global_store_dwordx4 v[32:33], v[8:11], off
	s_waitcnt vmcnt(15)
	s_nop 0
	v_lshlrev_b32_e32 v8, 16, v240
	v_and_b32_e32 v9, 0xffff0000, v240
	v_lshlrev_b32_e32 v10, 16, v241
	v_and_b32_e32 v11, 0xffff0000, v241
	v_lshlrev_b32_e32 v12, 16, v242
	v_and_b32_e32 v13, 0xffff0000, v242
	v_lshlrev_b32_e32 v14, 16, v243
	v_and_b32_e32 v15, 0xffff0000, v243
	v_pk_fma_f32 v[4:5], v[4:5], v[124:125], v[8:9]
	v_pk_fma_f32 v[8:9], v[2:3], v[122:123], v[14:15]
	v_pk_fma_f32 v[2:3], v[0:1], v[120:121], v[12:13]
	v_pk_fma_f32 v[6:7], v[6:7], v[126:127], v[10:11]
	v_cvt_pk_bf16_f32 v0, v4, v5
	s_nop 0
	v_cvt_pk_bf16_f32 v1, v6, v7
	v_cvt_pk_bf16_f32 v2, v2, v3
	v_cvt_pk_bf16_f32 v3, v8, v9
	global_store_dwordx4 v[24:25], v[0:3], off offset:256
	s_and_saveexec_b64 s[52:53], s[2:3]
	s_cbranch_execz .LBB0_2794
	s_andn2_b64 vcc, exec, s[12:13]
	s_cbranch_vccnz .LBB0_2793
	s_barrier
	s_branch .LBB0_2793
